# baseline (speedup 1.0000x reference)
_Z8moe_gemmILi1024ELi2048ELb1EEvPKDF16_S1_PKfPDF16_PfPKiS7_:
	v_lshl_or_b32 v216, s2, 8, v0
	v_and_b32_e32 v217, 63, v216
	v_lshrrev_b32_e32 v216, 6, v216
	v_lshlrev_b32_e32 v215, 3, v217
	v_and_b32_e32 v213, 1, v217
	v_mul_u32_u24_e32 v213, 0x1f8, v213
	v_add_u32_e32 v215, v215, v213
	v_lshlrev_b32_e32 v214, 4, v217
	v_lshl_add_u32 v217, v216, 10, v215
	v_lshl_add_u32 v216, v216, 11, v214
	s_mov_b32 s100, 0xaaaaaaaa
	s_mov_b32 s101, 0xaaaaaaaa
	s_mov_b32 s96, 16
	s_mov_b32 s97, 0
	s_mov_b32 s98, 0
	s_and_b32 s90, s2, 7
	s_lshr_b32 s91, s2, 3
	v_readfirstlane_b32 s88, v0
	s_load_dwordx2 s[4:5], s[0:1], 0x28
	v_readfirstlane_b32 s12, v0
	s_waitcnt lgkmcnt(0)
	s_load_dwordx2 s[92:93], s[4:5], 0x400
	s_add_u32 s94, s4, 0x6000000
	s_addc_u32 s95, s5, 0
	s_load_dword s23, s[4:5], 0x0
	s_load_dword s25, s[4:5], 0x80
	s_load_dword s27, s[4:5], 0x100
	s_load_dword s29, s[4:5], 0x180
	s_load_dword s31, s[4:5], 0x200
	s_load_dword s33, s[4:5], 0x280
	s_load_dword s35, s[4:5], 0x300
	s_load_dword s38, s[4:5], 0x380
	s_waitcnt lgkmcnt(0)
	s_add_i32 s3, s23, 0x9f
	s_mul_hi_i32 s3, s3, 0x66666667
	s_lshr_b32 s4, s3, 31
	s_ashr_i32 s39, s3, 6
	s_add_i32 s3, s25, 0x9f
	s_mul_hi_i32 s3, s3, 0x66666667
	s_add_i32 s39, s39, s4
	s_lshr_b32 s4, s3, 31
	s_ashr_i32 s40, s3, 6
	s_add_i32 s40, s40, s4
	s_add_i32 s4, s27, 0x9f
	s_mul_hi_i32 s4, s4, 0x66666667
	s_lshr_b32 s5, s4, 31
	s_ashr_i32 s41, s4, 6
	s_add_i32 s4, s29, 0x9f
	s_mul_hi_i32 s4, s4, 0x66666667
	s_add_i32 s41, s41, s5
	s_lshr_b32 s5, s4, 31
	s_ashr_i32 s42, s4, 6
	s_add_i32 s4, s31, 0x9f
	s_mul_hi_i32 s4, s4, 0x66666667
	s_add_i32 s42, s42, s5
	s_lshr_b32 s5, s4, 31
	s_ashr_i32 s43, s4, 6
	s_add_i32 s4, s33, 0x9f
	s_mul_hi_i32 s4, s4, 0x66666667
	s_add_i32 s3, s40, s39
	s_add_i32 s43, s43, s5
	s_lshr_b32 s5, s4, 31
	s_ashr_i32 s44, s4, 6
	s_add_i32 s4, s35, 0x9f
	s_add_i32 s3, s41, s3
	s_mul_hi_i32 s4, s4, 0x66666667
	s_add_i32 s3, s42, s3
	s_add_i32 s44, s44, s5
	s_lshr_b32 s5, s4, 31
	s_ashr_i32 s45, s4, 6
	s_add_i32 s4, s38, 0x9f
	s_add_i32 s3, s43, s3
	s_mul_hi_i32 s4, s4, 0x66666667
	s_add_i32 s3, s44, s3
	s_add_i32 s45, s45, s5
	s_lshr_b32 s5, s4, 31
	s_ashr_i32 s46, s4, 6
	s_add_i32 s3, s45, s3
	s_add_i32 s46, s46, s5
	s_add_i32 s3, s46, s3
	s_lshl_b32 s3, s3, 4
	s_and_b32 s4, s2, 7
	s_mul_i32 s4, s3, s4
	s_lshr_b32 s2, s2, 3
	s_ashr_i32 s5, s4, 3
	s_add_i32 s4, s4, s3
	s_ashr_i32 s47, s4, 3
	s_add_i32 s48, s5, s2
	s_sub_i32 s89, s47, s5
	s_sub_i32 s89, s89, 64
	s_max_i32 s89, s89, 0
	s_min_i32 s89, s89, 64
	s_add_i32 s99, s48, 64
	s_cmp_lt_i32 s99, s47
	s_cselect_b32 s98, 1, 0
	s_cmp_eq_u32 s98, 0
	s_cbranch_scc1 .Las_set
	s_cmp_ge_i32 s89, 64
	s_cbranch_scc1 .Las_set
	s_mov_b32 s96, 8
	s_mov_b32 s98, 3

.Lw2k_w1:
	s_barrier
	ds_read_b128 v[162:165], v178
	ds_read_b128 v[166:169], v178 offset:4096
	ds_read_b128 v[170:173], v174 offset:6144
	ds_read_b128 v[174:177], v174 offset:2048
	ds_read_b128 v[178:181], v178 offset:8192
	ds_read_b64_tr_b16 v[182:183], v200 offset:0
	ds_read_b64_tr_b16 v[184:185], v200 offset:0x400
	ds_read_b64_tr_b16 v[186:187], v201 offset:0
	ds_read_b64_tr_b16 v[188:189], v201 offset:0x400
	ds_read_b64_tr_b16 v[190:191], v202 offset:0
	ds_read_b64_tr_b16 v[192:193], v202 offset:0x400
	ds_read_b64_tr_b16 v[194:195], v203 offset:0
	ds_read_b64_tr_b16 v[196:197], v203 offset:0x400
	global_load_lds_dwordx4 v[120:121], off sc1
	v_lshl_add_u64 v[198:199], v[120:121], 0, s[16:17]
	s_mov_b32 m0, s14
	v_readfirstlane_b32 s14, v205
	v_add_u32_e32 v205, 0x8000, v204
	global_load_lds_dwordx4 v[198:199], off sc1
	v_lshl_add_u64 v[198:199], v[120:121], 0, s[18:19]
	s_mov_b32 m0, s14
	v_readfirstlane_b32 s14, v205
	global_load_lds_dwordx4 v[198:199], off sc1
	v_lshl_add_u64 v[198:199], v[120:121], 0, s[20:21]
	s_mov_b32 m0, s14
	s_nop 0
	global_load_lds_dwordx4 v[198:199], off sc1
	s_waitcnt lgkmcnt(0)
	s_setprio 1
	s_waitcnt lgkmcnt(0)
	v_mfma_f32_16x16x32_f16 v[92:95], v[182:185], v[162:165], v[92:95]
	v_mfma_f32_16x16x32_f16 v[88:91], v[186:189], v[162:165], v[88:91]
	v_mfma_f32_16x16x32_f16 v[84:87], v[190:193], v[162:165], v[84:87]
	v_mfma_f32_16x16x32_f16 v[80:83], v[194:197], v[162:165], v[80:83]
	v_mfma_f32_16x16x32_f16 v[76:79], v[182:185], v[174:177], v[76:79]
	v_mfma_f32_16x16x32_f16 v[72:75], v[186:189], v[174:177], v[72:75]
	v_mfma_f32_16x16x32_f16 v[68:71], v[190:193], v[174:177], v[68:71]
	v_mfma_f32_16x16x32_f16 v[64:67], v[194:197], v[174:177], v[64:67]
	v_mfma_f32_16x16x32_f16 v[60:63], v[182:185], v[166:169], v[60:63]
	v_mfma_f32_16x16x32_f16 v[56:59], v[186:189], v[166:169], v[56:59]
	v_mfma_f32_16x16x32_f16 v[52:55], v[190:193], v[166:169], v[52:55]
	v_mfma_f32_16x16x32_f16 v[48:51], v[194:197], v[166:169], v[48:51]
	v_mfma_f32_16x16x32_f16 v[44:47], v[182:185], v[170:173], v[44:47]
	v_mfma_f32_16x16x32_f16 v[40:43], v[186:189], v[170:173], v[40:43]
	v_mfma_f32_16x16x32_f16 v[36:39], v[190:193], v[170:173], v[36:39]
	v_mfma_f32_16x16x32_f16 v[32:35], v[194:197], v[170:173], v[32:35]
	v_mfma_f32_16x16x32_f16 v[28:31], v[182:185], v[178:181], v[28:31]
	v_mfma_f32_16x16x32_f16 v[24:27], v[186:189], v[178:181], v[24:27]
	v_mfma_f32_16x16x32_f16 v[20:23], v[190:193], v[178:181], v[20:23]
	v_mfma_f32_16x16x32_f16 v[16:19], v[194:197], v[178:181], v[16:19]
	s_setprio 0
	v_add_u32_e32 v178, v161, v158
	v_add_u32_e32 v161, v161, v157
	ds_read_b128 v[162:165], v178
	ds_read_b128 v[166:169], v178 offset:4096
	ds_read_b128 v[170:173], v161 offset:6144
	ds_read_b128 v[174:177], v161 offset:2048
	ds_read_b128 v[178:181], v178 offset:8192
	v_readfirstlane_b32 s14, v204
	v_add_u32_e32 v161, 0x1000, v204
	v_lshl_add_u64 v[198:199], v[112:113], 0, s[0:1]
	s_mov_b32 m0, s14
	v_readfirstlane_b32 s14, v161
	v_add_u32_e32 v161, 0x2000, v204
	ds_read_b64_tr_b16 v[182:183], v200 offset:0x2000
	ds_read_b64_tr_b16 v[184:185], v200 offset:0x2400
	ds_read_b64_tr_b16 v[186:187], v201 offset:0x2000
	ds_read_b64_tr_b16 v[188:189], v201 offset:0x2400
	ds_read_b64_tr_b16 v[190:191], v202 offset:0x2000
	ds_read_b64_tr_b16 v[192:193], v202 offset:0x2400
	ds_read_b64_tr_b16 v[194:195], v203 offset:0x2000
	ds_read_b64_tr_b16 v[196:197], v203 offset:0x2400
	global_load_lds_dwordx4 v[198:199], off sc1
	v_lshl_add_u64 v[198:199], v[114:115], 0, s[0:1]
	s_mov_b32 m0, s14
	v_readfirstlane_b32 s14, v161
	v_add_u32_e32 v161, 0x3000, v204
	global_load_lds_dwordx4 v[198:199], off sc1
	v_lshl_add_u64 v[198:199], v[116:117], 0, s[0:1]
	s_mov_b32 m0, s14
	v_readfirstlane_b32 s14, v161
	v_add_u32_e32 v161, 0x4000, v204
	global_load_lds_dwordx4 v[198:199], off sc1
	v_lshl_add_u64 v[198:199], v[118:119], 0, s[0:1]
	s_mov_b32 m0, s14
	v_readfirstlane_b32 s14, v161
	global_load_lds_dwordx4 v[198:199], off sc1
	v_lshl_add_u64 v[198:199], v[122:123], 0, s[0:1]
	s_mov_b32 m0, s14
	s_nop 0
	global_load_lds_dwordx4 v[198:199], off sc1
	s_waitcnt lgkmcnt(0)
	s_setprio 1
	s_waitcnt lgkmcnt(0)
	v_mfma_f32_16x16x32_f16 v[92:95], v[182:185], v[162:165], v[92:95]
	v_mfma_f32_16x16x32_f16 v[88:91], v[186:189], v[162:165], v[88:91]
	v_mfma_f32_16x16x32_f16 v[84:87], v[190:193], v[162:165], v[84:87]
	v_mfma_f32_16x16x32_f16 v[80:83], v[194:197], v[162:165], v[80:83]
	v_mfma_f32_16x16x32_f16 v[76:79], v[182:185], v[174:177], v[76:79]
	v_mfma_f32_16x16x32_f16 v[72:75], v[186:189], v[174:177], v[72:75]
	v_mfma_f32_16x16x32_f16 v[68:71], v[190:193], v[174:177], v[68:71]
	v_mfma_f32_16x16x32_f16 v[64:67], v[194:197], v[174:177], v[64:67]
	v_mfma_f32_16x16x32_f16 v[60:63], v[182:185], v[166:169], v[60:63]
	v_mfma_f32_16x16x32_f16 v[56:59], v[186:189], v[166:169], v[56:59]
	v_mfma_f32_16x16x32_f16 v[52:55], v[190:193], v[166:169], v[52:55]
	v_mfma_f32_16x16x32_f16 v[48:51], v[194:197], v[166:169], v[48:51]
	v_mfma_f32_16x16x32_f16 v[44:47], v[182:185], v[170:173], v[44:47]
	v_mfma_f32_16x16x32_f16 v[40:43], v[186:189], v[170:173], v[40:43]
	v_mfma_f32_16x16x32_f16 v[36:39], v[190:193], v[170:173], v[36:39]
	v_mfma_f32_16x16x32_f16 v[32:35], v[194:197], v[170:173], v[32:35]
	v_mfma_f32_16x16x32_f16 v[28:31], v[182:185], v[178:181], v[28:31]
	v_mfma_f32_16x16x32_f16 v[24:27], v[186:189], v[178:181], v[24:27]
	v_mfma_f32_16x16x32_f16 v[20:23], v[190:193], v[178:181], v[20:23]
	v_mfma_f32_16x16x32_f16 v[16:19], v[194:197], v[178:181], v[16:19]
	s_setprio 0
	s_cmp_eq_u32 s97, 0
	s_cbranch_scc1 .Lw2k_noc
	s_waitcnt vmcnt(9)
	v_cvt_pk_f16_f32 v208, v208, v209
	v_cvt_pk_f16_f32 v209, v210, v211
	v_cvt_pk_f16_f32 v210, v212, v213
	v_cvt_pk_f16_f32 v211, v214, v215
	v_mov_b32_dpp v212, v208 quad_perm:[1,0,3,2] row_mask:0xf bank_mask:0xf
	v_mov_b32_dpp v213, v209 quad_perm:[1,0,3,2] row_mask:0xf bank_mask:0xf
	v_mov_b32_dpp v214, v210 quad_perm:[1,0,3,2] row_mask:0xf bank_mask:0xf
	v_mov_b32_dpp v215, v211 quad_perm:[1,0,3,2] row_mask:0xf bank_mask:0xf
	v_cndmask_b32_e64 v208, v208, v214, s[100:101]
	v_cndmask_b32_e64 v209, v209, v215, s[100:101]
	v_cndmask_b32_e64 v210, v212, v210, s[100:101]
	v_cndmask_b32_e64 v211, v213, v211, s[100:101]
	global_store_dwordx4 v217, v[208:211], s[94:95]
	s_add_u32 s94, s94, 0x200000
	s_addc_u32 s95, s95, 0
	s_mov_b32 s97, 0

.Lw2k_nol:
	s_add_u32 s0, s0, 0x80
	s_addc_u32 s1, s1, 0
	s_add_i32 s80, s80, 1
	s_cmpk_lg_i32 s0, 0x780
	v_lshl_add_u64 v[120:121], v[120:121], 0, s[4:5]
	s_cbranch_scc1 .LBB2_45
	v_add_u32_e32 v159, v156, v159
	v_add_u32_e32 v160, v156, v160
	s_waitcnt vmcnt(0)
	s_waitcnt vmcnt(0)
	s_barrier
	s_cmp_eq_u32 s97, 0
	s_cbranch_scc1 .Lw2k_p0
	v_cvt_pk_f16_f32 v208, v208, v209
	v_cvt_pk_f16_f32 v209, v210, v211
	v_cvt_pk_f16_f32 v210, v212, v213
	v_cvt_pk_f16_f32 v211, v214, v215
	v_mov_b32_dpp v212, v208 quad_perm:[1,0,3,2] row_mask:0xf bank_mask:0xf
	v_mov_b32_dpp v213, v209 quad_perm:[1,0,3,2] row_mask:0xf bank_mask:0xf
	v_mov_b32_dpp v214, v210 quad_perm:[1,0,3,2] row_mask:0xf bank_mask:0xf
	v_mov_b32_dpp v215, v211 quad_perm:[1,0,3,2] row_mask:0xf bank_mask:0xf
	v_cndmask_b32_e64 v208, v208, v214, s[100:101]
	v_cndmask_b32_e64 v209, v209, v215, s[100:101]
	v_cndmask_b32_e64 v210, v212, v210, s[100:101]
	v_cndmask_b32_e64 v211, v213, v211, s[100:101]
	global_store_dwordx4 v217, v[208:211], s[94:95]
	s_add_u32 s94, s94, 0x200000
	s_addc_u32 s95, s95, 0
	s_mov_b32 s97, 0

.Lw2k_tissued:
	s_waitcnt vmcnt(0)
	s_cmp_le_u32 s26, 0
	s_cbranch_scc1 .Lw2k_tstored
	v_cvt_pk_f16_f32 v8, v8, v9
	v_cvt_pk_f16_f32 v9, v10, v11
	v_cvt_pk_f16_f32 v10, v12, v13
	v_cvt_pk_f16_f32 v11, v14, v15
	v_mov_b32_dpp v12, v8 quad_perm:[1,0,3,2] row_mask:0xf bank_mask:0xf
	v_mov_b32_dpp v13, v9 quad_perm:[1,0,3,2] row_mask:0xf bank_mask:0xf
	v_mov_b32_dpp v14, v10 quad_perm:[1,0,3,2] row_mask:0xf bank_mask:0xf
	v_mov_b32_dpp v15, v11 quad_perm:[1,0,3,2] row_mask:0xf bank_mask:0xf
	v_cndmask_b32_e64 v8, v8, v14, s[100:101]
	v_cndmask_b32_e64 v9, v9, v15, s[100:101]
	v_cndmask_b32_e64 v10, v12, v10, s[100:101]
	v_cndmask_b32_e64 v11, v13, v11, s[100:101]
	global_store_dwordx4 v217, v[8:11], s[32:33]
	s_cmp_le_u32 s26, 1
	s_cbranch_scc1 .Lw2k_tstored
	v_cvt_pk_f16_f32 v16, v16, v17
	v_cvt_pk_f16_f32 v17, v18, v19
	v_cvt_pk_f16_f32 v18, v20, v21
	v_cvt_pk_f16_f32 v19, v22, v23
	v_mov_b32_dpp v20, v16 quad_perm:[1,0,3,2] row_mask:0xf bank_mask:0xf
	v_mov_b32_dpp v21, v17 quad_perm:[1,0,3,2] row_mask:0xf bank_mask:0xf
	v_mov_b32_dpp v22, v18 quad_perm:[1,0,3,2] row_mask:0xf bank_mask:0xf
	v_mov_b32_dpp v23, v19 quad_perm:[1,0,3,2] row_mask:0xf bank_mask:0xf
	v_cndmask_b32_e64 v16, v16, v22, s[100:101]
	v_cndmask_b32_e64 v17, v17, v23, s[100:101]
	v_cndmask_b32_e64 v18, v20, v18, s[100:101]
	v_cndmask_b32_e64 v19, v21, v19, s[100:101]
	global_store_dwordx4 v217, v[16:19], s[36:37]
	s_cmp_le_u32 s26, 2
	s_cbranch_scc1 .Lw2k_tstored
	v_cvt_pk_f16_f32 v24, v24, v25
	v_cvt_pk_f16_f32 v25, v26, v27
	v_cvt_pk_f16_f32 v26, v28, v29
	v_cvt_pk_f16_f32 v27, v30, v31
	v_mov_b32_dpp v28, v24 quad_perm:[1,0,3,2] row_mask:0xf bank_mask:0xf
	v_mov_b32_dpp v29, v25 quad_perm:[1,0,3,2] row_mask:0xf bank_mask:0xf
	v_mov_b32_dpp v30, v26 quad_perm:[1,0,3,2] row_mask:0xf bank_mask:0xf
	v_mov_b32_dpp v31, v27 quad_perm:[1,0,3,2] row_mask:0xf bank_mask:0xf
	v_cndmask_b32_e64 v24, v24, v30, s[100:101]
	v_cndmask_b32_e64 v25, v25, v31, s[100:101]
	v_cndmask_b32_e64 v26, v28, v26, s[100:101]
	v_cndmask_b32_e64 v27, v29, v27, s[100:101]
	global_store_dwordx4 v217, v[24:27], s[40:41]
	s_cmp_le_u32 s26, 3
	s_cbranch_scc1 .Lw2k_tstored
	v_cvt_pk_f16_f32 v32, v32, v33
	v_cvt_pk_f16_f32 v33, v34, v35
	v_cvt_pk_f16_f32 v34, v36, v37
	v_cvt_pk_f16_f32 v35, v38, v39
	v_mov_b32_dpp v36, v32 quad_perm:[1,0,3,2] row_mask:0xf bank_mask:0xf
	v_mov_b32_dpp v37, v33 quad_perm:[1,0,3,2] row_mask:0xf bank_mask:0xf
	v_mov_b32_dpp v38, v34 quad_perm:[1,0,3,2] row_mask:0xf bank_mask:0xf
	v_mov_b32_dpp v39, v35 quad_perm:[1,0,3,2] row_mask:0xf bank_mask:0xf
	v_cndmask_b32_e64 v32, v32, v38, s[100:101]
	v_cndmask_b32_e64 v33, v33, v39, s[100:101]
	v_cndmask_b32_e64 v34, v36, v34, s[100:101]
	v_cndmask_b32_e64 v35, v37, v35, s[100:101]
	global_store_dwordx4 v217, v[32:35], s[44:45]
	s_cmp_le_u32 s26, 4
	s_cbranch_scc1 .Lw2k_tstored
	v_cvt_pk_f16_f32 v40, v40, v41
	v_cvt_pk_f16_f32 v41, v42, v43
	v_cvt_pk_f16_f32 v42, v44, v45
	v_cvt_pk_f16_f32 v43, v46, v47
	v_mov_b32_dpp v44, v40 quad_perm:[1,0,3,2] row_mask:0xf bank_mask:0xf
	v_mov_b32_dpp v45, v41 quad_perm:[1,0,3,2] row_mask:0xf bank_mask:0xf
	v_mov_b32_dpp v46, v42 quad_perm:[1,0,3,2] row_mask:0xf bank_mask:0xf
	v_mov_b32_dpp v47, v43 quad_perm:[1,0,3,2] row_mask:0xf bank_mask:0xf
	v_cndmask_b32_e64 v40, v40, v46, s[100:101]
	v_cndmask_b32_e64 v41, v41, v47, s[100:101]
	v_cndmask_b32_e64 v42, v44, v42, s[100:101]
	v_cndmask_b32_e64 v43, v45, v43, s[100:101]
	global_store_dwordx4 v217, v[40:43], s[48:49]
	s_cmp_le_u32 s26, 5
	s_cbranch_scc1 .Lw2k_tstored
	v_cvt_pk_f16_f32 v48, v48, v49
	v_cvt_pk_f16_f32 v49, v50, v51
	v_cvt_pk_f16_f32 v50, v52, v53
	v_cvt_pk_f16_f32 v51, v54, v55
	v_mov_b32_dpp v52, v48 quad_perm:[1,0,3,2] row_mask:0xf bank_mask:0xf
	v_mov_b32_dpp v53, v49 quad_perm:[1,0,3,2] row_mask:0xf bank_mask:0xf
	v_mov_b32_dpp v54, v50 quad_perm:[1,0,3,2] row_mask:0xf bank_mask:0xf
	v_mov_b32_dpp v55, v51 quad_perm:[1,0,3,2] row_mask:0xf bank_mask:0xf
	v_cndmask_b32_e64 v48, v48, v54, s[100:101]
	v_cndmask_b32_e64 v49, v49, v55, s[100:101]
	v_cndmask_b32_e64 v50, v52, v50, s[100:101]
	v_cndmask_b32_e64 v51, v53, v51, s[100:101]
	global_store_dwordx4 v217, v[48:51], s[52:53]
	s_cmp_le_u32 s26, 6
	s_cbranch_scc1 .Lw2k_tstored
	v_cvt_pk_f16_f32 v56, v56, v57
	v_cvt_pk_f16_f32 v57, v58, v59
	v_cvt_pk_f16_f32 v58, v60, v61
	v_cvt_pk_f16_f32 v59, v62, v63
	v_mov_b32_dpp v60, v56 quad_perm:[1,0,3,2] row_mask:0xf bank_mask:0xf
	v_mov_b32_dpp v61, v57 quad_perm:[1,0,3,2] row_mask:0xf bank_mask:0xf
	v_mov_b32_dpp v62, v58 quad_perm:[1,0,3,2] row_mask:0xf bank_mask:0xf
	v_mov_b32_dpp v63, v59 quad_perm:[1,0,3,2] row_mask:0xf bank_mask:0xf
	v_cndmask_b32_e64 v56, v56, v62, s[100:101]
	v_cndmask_b32_e64 v57, v57, v63, s[100:101]
	v_cndmask_b32_e64 v58, v60, v58, s[100:101]
	v_cndmask_b32_e64 v59, v61, v59, s[100:101]
	global_store_dwordx4 v217, v[56:59], s[56:57]
	s_cmp_le_u32 s26, 7
	s_cbranch_scc1 .Lw2k_tstored
	v_cvt_pk_f16_f32 v64, v64, v65
	v_cvt_pk_f16_f32 v65, v66, v67
	v_cvt_pk_f16_f32 v66, v68, v69
	v_cvt_pk_f16_f32 v67, v70, v71
	v_mov_b32_dpp v68, v64 quad_perm:[1,0,3,2] row_mask:0xf bank_mask:0xf
	v_mov_b32_dpp v69, v65 quad_perm:[1,0,3,2] row_mask:0xf bank_mask:0xf
	v_mov_b32_dpp v70, v66 quad_perm:[1,0,3,2] row_mask:0xf bank_mask:0xf
	v_mov_b32_dpp v71, v67 quad_perm:[1,0,3,2] row_mask:0xf bank_mask:0xf
	v_cndmask_b32_e64 v64, v64, v70, s[100:101]
	v_cndmask_b32_e64 v65, v65, v71, s[100:101]
	v_cndmask_b32_e64 v66, v68, v66, s[100:101]
	v_cndmask_b32_e64 v67, v69, v67, s[100:101]
	global_store_dwordx4 v217, v[64:67], s[60:61]

.Lw2k_end:
	s_cmp_lg_u32 s98, 0
	s_cbranch_scc1 .Las_end
	s_cmp_eq_u32 s89, 0
	s_cbranch_scc1 .Las_end
	s_cmp_ge_i32 s89, 64
	s_cbranch_scc1 .Las_end
	s_sub_i32 s20, s91, s89
	s_sub_i32 s27, 64, s89
	s_lshl_b32 s28, s89, 3
	s_lshr_b32 s29, s88, 6
	s_sub_u32 s64, s92, 0x4000000
	s_subb_u32 s65, s93, 0
	s_sub_u32 s66, s94, 0x2000000
	s_subb_u32 s67, s95, 0
	v_mbcnt_lo_u32_b32 v0, -1, 0
	v_mbcnt_hi_u32_b32 v0, -1, v0
	v_lshlrev_b32_e32 v1, 4, v0
	v_lshlrev_b32_e32 v2, 3, v0
	v_and_b32_e32 v3, 1, v0
	v_mul_u32_u24_e32 v3, 0x1f8, v3
	v_add_u32_e32 v2, v2, v3

.Las_issued:
	s_waitcnt vmcnt(0)
	s_cmp_le_u32 s26, 0
	s_cbranch_scc1 .Las_stored
	v_cvt_pk_f16_f32 v8, v8, v9
	v_cvt_pk_f16_f32 v9, v10, v11
	v_cvt_pk_f16_f32 v10, v12, v13
	v_cvt_pk_f16_f32 v11, v14, v15
	v_mov_b32_dpp v12, v8 quad_perm:[1,0,3,2] row_mask:0xf bank_mask:0xf
	v_mov_b32_dpp v13, v9 quad_perm:[1,0,3,2] row_mask:0xf bank_mask:0xf
	v_mov_b32_dpp v14, v10 quad_perm:[1,0,3,2] row_mask:0xf bank_mask:0xf
	v_mov_b32_dpp v15, v11 quad_perm:[1,0,3,2] row_mask:0xf bank_mask:0xf
	v_cndmask_b32_e64 v8, v8, v14, s[100:101]
	v_cndmask_b32_e64 v9, v9, v15, s[100:101]
	v_cndmask_b32_e64 v10, v12, v10, s[100:101]
	v_cndmask_b32_e64 v11, v13, v11, s[100:101]
	global_store_dwordx4 v2, v[8:11], s[32:33]
	s_cmp_le_u32 s26, 1
	s_cbranch_scc1 .Las_stored
	v_cvt_pk_f16_f32 v16, v16, v17
	v_cvt_pk_f16_f32 v17, v18, v19
	v_cvt_pk_f16_f32 v18, v20, v21
	v_cvt_pk_f16_f32 v19, v22, v23
	v_mov_b32_dpp v20, v16 quad_perm:[1,0,3,2] row_mask:0xf bank_mask:0xf
	v_mov_b32_dpp v21, v17 quad_perm:[1,0,3,2] row_mask:0xf bank_mask:0xf
	v_mov_b32_dpp v22, v18 quad_perm:[1,0,3,2] row_mask:0xf bank_mask:0xf
	v_mov_b32_dpp v23, v19 quad_perm:[1,0,3,2] row_mask:0xf bank_mask:0xf
	v_cndmask_b32_e64 v16, v16, v22, s[100:101]
	v_cndmask_b32_e64 v17, v17, v23, s[100:101]
	v_cndmask_b32_e64 v18, v20, v18, s[100:101]
	v_cndmask_b32_e64 v19, v21, v19, s[100:101]
	global_store_dwordx4 v2, v[16:19], s[36:37]
	s_cmp_le_u32 s26, 2
	s_cbranch_scc1 .Las_stored
	v_cvt_pk_f16_f32 v24, v24, v25
	v_cvt_pk_f16_f32 v25, v26, v27
	v_cvt_pk_f16_f32 v26, v28, v29
	v_cvt_pk_f16_f32 v27, v30, v31
	v_mov_b32_dpp v28, v24 quad_perm:[1,0,3,2] row_mask:0xf bank_mask:0xf
	v_mov_b32_dpp v29, v25 quad_perm:[1,0,3,2] row_mask:0xf bank_mask:0xf
	v_mov_b32_dpp v30, v26 quad_perm:[1,0,3,2] row_mask:0xf bank_mask:0xf
	v_mov_b32_dpp v31, v27 quad_perm:[1,0,3,2] row_mask:0xf bank_mask:0xf
	v_cndmask_b32_e64 v24, v24, v30, s[100:101]
	v_cndmask_b32_e64 v25, v25, v31, s[100:101]
	v_cndmask_b32_e64 v26, v28, v26, s[100:101]
	v_cndmask_b32_e64 v27, v29, v27, s[100:101]
	global_store_dwordx4 v2, v[24:27], s[40:41]
	s_cmp_le_u32 s26, 3
	s_cbranch_scc1 .Las_stored
	v_cvt_pk_f16_f32 v32, v32, v33
	v_cvt_pk_f16_f32 v33, v34, v35
	v_cvt_pk_f16_f32 v34, v36, v37
	v_cvt_pk_f16_f32 v35, v38, v39
	v_mov_b32_dpp v36, v32 quad_perm:[1,0,3,2] row_mask:0xf bank_mask:0xf
	v_mov_b32_dpp v37, v33 quad_perm:[1,0,3,2] row_mask:0xf bank_mask:0xf
	v_mov_b32_dpp v38, v34 quad_perm:[1,0,3,2] row_mask:0xf bank_mask:0xf
	v_mov_b32_dpp v39, v35 quad_perm:[1,0,3,2] row_mask:0xf bank_mask:0xf
	v_cndmask_b32_e64 v32, v32, v38, s[100:101]
	v_cndmask_b32_e64 v33, v33, v39, s[100:101]
	v_cndmask_b32_e64 v34, v36, v34, s[100:101]
	v_cndmask_b32_e64 v35, v37, v35, s[100:101]
	global_store_dwordx4 v2, v[32:35], s[44:45]
	s_cmp_le_u32 s26, 4
	s_cbranch_scc1 .Las_stored
	v_cvt_pk_f16_f32 v40, v40, v41
	v_cvt_pk_f16_f32 v41, v42, v43
	v_cvt_pk_f16_f32 v42, v44, v45
	v_cvt_pk_f16_f32 v43, v46, v47
	v_mov_b32_dpp v44, v40 quad_perm:[1,0,3,2] row_mask:0xf bank_mask:0xf
	v_mov_b32_dpp v45, v41 quad_perm:[1,0,3,2] row_mask:0xf bank_mask:0xf
	v_mov_b32_dpp v46, v42 quad_perm:[1,0,3,2] row_mask:0xf bank_mask:0xf
	v_mov_b32_dpp v47, v43 quad_perm:[1,0,3,2] row_mask:0xf bank_mask:0xf
	v_cndmask_b32_e64 v40, v40, v46, s[100:101]
	v_cndmask_b32_e64 v41, v41, v47, s[100:101]
	v_cndmask_b32_e64 v42, v44, v42, s[100:101]
	v_cndmask_b32_e64 v43, v45, v43, s[100:101]
	global_store_dwordx4 v2, v[40:43], s[48:49]
	s_cmp_le_u32 s26, 5
	s_cbranch_scc1 .Las_stored
	v_cvt_pk_f16_f32 v48, v48, v49
	v_cvt_pk_f16_f32 v49, v50, v51
	v_cvt_pk_f16_f32 v50, v52, v53
	v_cvt_pk_f16_f32 v51, v54, v55
	v_mov_b32_dpp v52, v48 quad_perm:[1,0,3,2] row_mask:0xf bank_mask:0xf
	v_mov_b32_dpp v53, v49 quad_perm:[1,0,3,2] row_mask:0xf bank_mask:0xf
	v_mov_b32_dpp v54, v50 quad_perm:[1,0,3,2] row_mask:0xf bank_mask:0xf
	v_mov_b32_dpp v55, v51 quad_perm:[1,0,3,2] row_mask:0xf bank_mask:0xf
	v_cndmask_b32_e64 v48, v48, v54, s[100:101]
	v_cndmask_b32_e64 v49, v49, v55, s[100:101]
	v_cndmask_b32_e64 v50, v52, v50, s[100:101]
	v_cndmask_b32_e64 v51, v53, v51, s[100:101]
	global_store_dwordx4 v2, v[48:51], s[52:53]
	s_cmp_le_u32 s26, 6
	s_cbranch_scc1 .Las_stored
	v_cvt_pk_f16_f32 v56, v56, v57
	v_cvt_pk_f16_f32 v57, v58, v59
	v_cvt_pk_f16_f32 v58, v60, v61
	v_cvt_pk_f16_f32 v59, v62, v63
	v_mov_b32_dpp v60, v56 quad_perm:[1,0,3,2] row_mask:0xf bank_mask:0xf
	v_mov_b32_dpp v61, v57 quad_perm:[1,0,3,2] row_mask:0xf bank_mask:0xf
	v_mov_b32_dpp v62, v58 quad_perm:[1,0,3,2] row_mask:0xf bank_mask:0xf
	v_mov_b32_dpp v63, v59 quad_perm:[1,0,3,2] row_mask:0xf bank_mask:0xf
	v_cndmask_b32_e64 v56, v56, v62, s[100:101]
	v_cndmask_b32_e64 v57, v57, v63, s[100:101]
	v_cndmask_b32_e64 v58, v60, v58, s[100:101]
	v_cndmask_b32_e64 v59, v61, v59, s[100:101]
	global_store_dwordx4 v2, v[56:59], s[56:57]
	s_cmp_le_u32 s26, 7
	s_cbranch_scc1 .Las_stored
	v_cvt_pk_f16_f32 v64, v64, v65
	v_cvt_pk_f16_f32 v65, v66, v67
	v_cvt_pk_f16_f32 v66, v68, v69
	v_cvt_pk_f16_f32 v67, v70, v71
	v_mov_b32_dpp v68, v64 quad_perm:[1,0,3,2] row_mask:0xf bank_mask:0xf
	v_mov_b32_dpp v69, v65 quad_perm:[1,0,3,2] row_mask:0xf bank_mask:0xf
	v_mov_b32_dpp v70, v66 quad_perm:[1,0,3,2] row_mask:0xf bank_mask:0xf
	v_mov_b32_dpp v71, v67 quad_perm:[1,0,3,2] row_mask:0xf bank_mask:0xf
	v_cndmask_b32_e64 v64, v64, v70, s[100:101]
	v_cndmask_b32_e64 v65, v65, v71, s[100:101]
	v_cndmask_b32_e64 v66, v68, v66, s[100:101]
	v_cndmask_b32_e64 v67, v69, v67, s[100:101]
	global_store_dwordx4 v2, v[64:67], s[60:61]

	.amdhsa_kernel _Z8moe_gemmILi1024ELi2048ELb1EEvPKDF16_S1_PKfPDF16_PfPKiS7_
		.amdhsa_group_segment_fixed_size 0
		.amdhsa_private_segment_fixed_size 0
		.amdhsa_kernarg_size 312
		.amdhsa_user_sgpr_count 2
		.amdhsa_user_sgpr_dispatch_ptr 0
		.amdhsa_user_sgpr_queue_ptr 0
		.amdhsa_user_sgpr_kernarg_segment_ptr 1
		.amdhsa_user_sgpr_dispatch_id 0
		.amdhsa_user_sgpr_kernarg_preload_length 0
		.amdhsa_user_sgpr_kernarg_preload_offset 0
		.amdhsa_user_sgpr_private_segment_size 0
		.amdhsa_uses_dynamic_stack 0
		.amdhsa_enable_private_segment 0
		.amdhsa_system_sgpr_workgroup_id_x 1
		.amdhsa_system_sgpr_workgroup_id_y 0
		.amdhsa_system_sgpr_workgroup_id_z 0
		.amdhsa_system_sgpr_workgroup_info 0
		.amdhsa_system_vgpr_workitem_id 0
		.amdhsa_next_free_vgpr 218
		.amdhsa_next_free_sgpr 102
		.amdhsa_accum_offset 220
		.amdhsa_reserve_vcc 1
		.amdhsa_float_round_mode_32 0
		.amdhsa_float_round_mode_16_64 0
		.amdhsa_float_denorm_mode_32 3
		.amdhsa_float_denorm_mode_16_64 3
		.amdhsa_dx10_clamp 1
		.amdhsa_ieee_mode 1
		.amdhsa_fp16_overflow 0
		.amdhsa_tg_split 0
		.amdhsa_exception_fp_ieee_invalid_op 0
		.amdhsa_exception_fp_denorm_src 0
		.amdhsa_exception_fp_ieee_div_zero 0
		.amdhsa_exception_fp_ieee_overflow 0
		.amdhsa_exception_fp_ieee_underflow 0
		.amdhsa_exception_fp_ieee_inexact 0
		.amdhsa_exception_int_div_zero 0
	.end_amdhsa_kernel

amdhsa.kernels:
  - .agpr_count:     0
    .args:
      - .actual_access:  read_only
        .address_space:  global
        .offset:         0
        .size:           8
        .value_kind:     global_buffer
      - .address_space:  global
        .offset:         8
        .size:           8
        .value_kind:     global_buffer
      - .actual_access:  read_only
        .address_space:  global
        .offset:         16
        .size:           8
        .value_kind:     global_buffer
      - .address_space:  global
        .offset:         24
        .size:           8
        .value_kind:     global_buffer
      - .offset:         32
        .size:           4
        .value_kind:     by_value
      - .actual_access:  write_only
        .address_space:  global
        .offset:         40
        .size:           8
        .value_kind:     global_buffer
      - .offset:         48
        .size:           4
        .value_kind:     hidden_block_count_x
      - .offset:         52
        .size:           4
        .value_kind:     hidden_block_count_y
      - .offset:         56
        .size:           4
        .value_kind:     hidden_block_count_z
      - .offset:         60
        .size:           2
        .value_kind:     hidden_group_size_x
      - .offset:         62
        .size:           2
        .value_kind:     hidden_group_size_y
      - .offset:         64
        .size:           2
        .value_kind:     hidden_group_size_z
      - .offset:         66
        .size:           2
        .value_kind:     hidden_remainder_x
      - .offset:         68
        .size:           2
        .value_kind:     hidden_remainder_y
      - .offset:         70
        .size:           2
        .value_kind:     hidden_remainder_z
      - .offset:         88
        .size:           8
        .value_kind:     hidden_global_offset_x
      - .offset:         96
        .size:           8
        .value_kind:     hidden_global_offset_y
      - .offset:         104
        .size:           8
        .value_kind:     hidden_global_offset_z
      - .offset:         112
        .size:           2
        .value_kind:     hidden_grid_dims
    .group_segment_fixed_size: 0
    .kernarg_segment_align: 8
    .kernarg_segment_size: 304
    .language:       OpenCL C
    .language_version:
      - 2
      - 0
    .max_flat_workgroup_size: 256
    .name:           _Z5cvt_wPKfPDF16_S0_S1_iPi
    .private_segment_fixed_size: 0
    .sgpr_count:     30
    .sgpr_spill_count: 0
    .symbol:         _Z5cvt_wPKfPDF16_S0_S1_iPi.kd
    .uniform_work_group_size: 1
    .uses_dynamic_stack: false
    .vgpr_count:     40
    .vgpr_spill_count: 0
    .wavefront_size: 64
  - .agpr_count:     0
    .args:
      - .actual_access:  read_only
        .address_space:  global
        .offset:         0
        .size:           8
        .value_kind:     global_buffer
      - .actual_access:  read_only
        .address_space:  global
        .offset:         8
        .size:           8
        .value_kind:     global_buffer
      - .actual_access:  read_only
        .address_space:  global
        .offset:         16
        .size:           8
        .value_kind:     global_buffer
      - .actual_access:  write_only
        .address_space:  global
        .offset:         24
        .size:           8
        .value_kind:     global_buffer
      - .address_space:  global
        .offset:         32
        .size:           8
        .value_kind:     global_buffer
      - .actual_access:  write_only
        .address_space:  global
        .offset:         40
        .size:           8
        .value_kind:     global_buffer
      - .actual_access:  write_only
        .address_space:  global
        .offset:         48
        .size:           8
        .value_kind:     global_buffer
      - .actual_access:  read_only
        .address_space:  global
        .offset:         56
        .size:           8
        .value_kind:     global_buffer
      - .address_space:  global
        .offset:         64
        .size:           8
        .value_kind:     global_buffer
      - .offset:         72
        .size:           4
        .value_kind:     by_value
      - .offset:         80
        .size:           4
        .value_kind:     hidden_block_count_x
      - .offset:         84
        .size:           4
        .value_kind:     hidden_block_count_y
      - .offset:         88
        .size:           4
        .value_kind:     hidden_block_count_z
      - .offset:         92
        .size:           2
        .value_kind:     hidden_group_size_x
      - .offset:         94
        .size:           2
        .value_kind:     hidden_group_size_y
      - .offset:         96
        .size:           2
        .value_kind:     hidden_group_size_z
      - .offset:         98
        .size:           2
        .value_kind:     hidden_remainder_x
      - .offset:         100
        .size:           2
        .value_kind:     hidden_remainder_y
      - .offset:         102
        .size:           2
        .value_kind:     hidden_remainder_z
      - .offset:         120
        .size:           8
        .value_kind:     hidden_global_offset_x
      - .offset:         128
        .size:           8
        .value_kind:     hidden_global_offset_y
      - .offset:         136
        .size:           8
        .value_kind:     hidden_global_offset_z
      - .offset:         144
        .size:           2
        .value_kind:     hidden_grid_dims
    .group_segment_fixed_size: 32928
    .kernarg_segment_align: 8
    .kernarg_segment_size: 336
    .language:       OpenCL C
    .language_version:
      - 2
      - 0
    .max_flat_workgroup_size: 512
    .name:           _Z11gate_kernelPKfS0_S0_PDF16_PiS2_PfS0_S1_i
    .private_segment_fixed_size: 0
    .sgpr_count:     66
    .sgpr_spill_count: 0
    .symbol:         _Z11gate_kernelPKfS0_S0_PDF16_PiS2_PfS0_S1_i.kd
    .uniform_work_group_size: 1
    .uses_dynamic_stack: false
    .vgpr_count:     115
    .vgpr_spill_count: 0
    .wavefront_size: 64
  - .agpr_count:     0
    .args:
      - .address_space:  global
        .offset:         0
        .size:           8
        .value_kind:     global_buffer
      - .address_space:  global
        .offset:         8
        .size:           8
        .value_kind:     global_buffer
      - .actual_access:  read_only
        .address_space:  global
        .offset:         16
        .size:           8
        .value_kind:     global_buffer
      - .address_space:  global
        .offset:         24
        .size:           8
        .value_kind:     global_buffer
      - .actual_access:  read_only
        .address_space:  global
        .offset:         32
        .size:           8
        .value_kind:     global_buffer
      - .actual_access:  read_only
        .address_space:  global
        .offset:         40
        .size:           8
        .value_kind:     global_buffer
      - .actual_access:  read_only
        .address_space:  global
        .offset:         48
        .size:           8
        .value_kind:     global_buffer
      - .offset:         56
        .size:           4
        .value_kind:     hidden_block_count_x
      - .offset:         60
        .size:           4
        .value_kind:     hidden_block_count_y
      - .offset:         64
        .size:           4
        .value_kind:     hidden_block_count_z
      - .offset:         68
        .size:           2
        .value_kind:     hidden_group_size_x
      - .offset:         70
        .size:           2
        .value_kind:     hidden_group_size_y
      - .offset:         72
        .size:           2
        .value_kind:     hidden_group_size_z
      - .offset:         74
        .size:           2
        .value_kind:     hidden_remainder_x
      - .offset:         76
        .size:           2
        .value_kind:     hidden_remainder_y
      - .offset:         78
        .size:           2
        .value_kind:     hidden_remainder_z
      - .offset:         96
        .size:           8
        .value_kind:     hidden_global_offset_x
      - .offset:         104
        .size:           8
        .value_kind:     hidden_global_offset_y
      - .offset:         112
        .size:           8
        .value_kind:     hidden_global_offset_z
      - .offset:         120
        .size:           2
        .value_kind:     hidden_grid_dims
      - .offset:         176
        .size:           4
        .value_kind:     hidden_dynamic_lds_size
    .group_segment_fixed_size: 0
    .kernarg_segment_align: 8
    .kernarg_segment_size: 312
    .language:       OpenCL C
    .language_version:
      - 2
      - 0
    .max_flat_workgroup_size: 256
    .name:           _Z8moe_gemmILi1024ELi2048ELb1EEvPKDF16_S1_PKfPDF16_PfPKiS7_
    .private_segment_fixed_size: 0
    .sgpr_count:     108
    .sgpr_spill_count: 0
    .symbol:         _Z8moe_gemmILi1024ELi2048ELb1EEvPKDF16_S1_PKfPDF16_PfPKiS7_.kd
    .uniform_work_group_size: 1
    .uses_dynamic_stack: false
    .vgpr_count:     218
    .vgpr_spill_count: 0
    .wavefront_size: 64
  - .agpr_count:     256
    .args:
      - .address_space:  global
        .offset:         0
        .size:           8
        .value_kind:     global_buffer
      - .address_space:  global
        .offset:         8
        .size:           8
        .value_kind:     global_buffer
      - .actual_access:  read_only
        .address_space:  global
        .offset:         16
        .size:           8
        .value_kind:     global_buffer
      - .actual_access:  read_only
        .address_space:  global
        .offset:         24
        .size:           8
        .value_kind:     global_buffer
      - .address_space:  global
        .offset:         32
        .size:           8
        .value_kind:     global_buffer
      - .actual_access:  read_only
        .address_space:  global
        .offset:         40
        .size:           8
        .value_kind:     global_buffer
      - .actual_access:  read_only
        .address_space:  global
        .offset:         48
        .size:           8
        .value_kind:     global_buffer
      - .offset:         56
        .size:           4
        .value_kind:     hidden_block_count_x
      - .offset:         60
        .size:           4
        .value_kind:     hidden_block_count_y
      - .offset:         64
        .size:           4
        .value_kind:     hidden_block_count_z
      - .offset:         68
        .size:           2
        .value_kind:     hidden_group_size_x
      - .offset:         70
        .size:           2
        .value_kind:     hidden_group_size_y
      - .offset:         72
        .size:           2
        .value_kind:     hidden_group_size_z
      - .offset:         74
        .size:           2
        .value_kind:     hidden_remainder_x
      - .offset:         76
        .size:           2
        .value_kind:     hidden_remainder_y
      - .offset:         78
        .size:           2
        .value_kind:     hidden_remainder_z
      - .offset:         96
        .size:           8
        .value_kind:     hidden_global_offset_x
      - .offset:         104
        .size:           8
        .value_kind:     hidden_global_offset_y
      - .offset:         112
        .size:           8
        .value_kind:     hidden_global_offset_z
      - .offset:         120
        .size:           2
        .value_kind:     hidden_grid_dims
      - .offset:         176
        .size:           4
        .value_kind:     hidden_dynamic_lds_size
    .group_segment_fixed_size: 86016
    .kernarg_segment_align: 8
    .kernarg_segment_size: 312
    .language:       OpenCL C
    .language_version:
      - 2
      - 0
    .max_flat_workgroup_size: 256
    .name:           _Z8moe_gemmILi2048ELi1024ELb0EEvPKDF16_S1_PKfPDF16_PfPKiS7_
    .private_segment_fixed_size: 0
    .sgpr_count:     96
    .sgpr_spill_count: 0
    .symbol:         _Z8moe_gemmILi2048ELi1024ELb0EEvPKDF16_S1_PKfPDF16_PfPKiS7_.kd
    .uniform_work_group_size: 1
    .uses_dynamic_stack: false
    .vgpr_count:     512
    .vgpr_spill_count: 0
    .wavefront_size: 64
